# P10: gf loads hoisted, full-line output stores via permlane32_swap, no nt; grid barrier: first arriver of each XCD issues an early L2 writeback
# speedup vs baseline: 1.0128x; 1.0128x over previous
.LBB0_157:
	s_or_b64 exec, exec, s[4:5]
	v_cvt_f32_u32_e32 v4, v2
	s_waitcnt vmcnt(0)
	v_readfirstlane_b32 s3, v3
	v_sub_u32_e32 v3, 0, v2
	v_rcp_iflag_f32_e32 v4, v4
	v_add_u32_e32 v5, s3, v1
	v_mul_f32_e32 v4, 0x4f7ffffe, v4
	v_cvt_u32_f32_e32 v4, v4
	v_mul_lo_u32 v1, v3, v4
	v_mul_hi_u32 v1, v4, v1
	v_add_u32_e32 v1, v4, v1
	v_mul_hi_u32 v1, v5, v1
	v_mul_lo_u32 v3, v1, v2
	v_sub_u32_e32 v3, v5, v3
	v_add_u32_e32 v4, 1, v1
	v_cmp_ge_u32_e32 vcc, v3, v2
	s_nop 1
	v_cndmask_b32_e32 v1, v1, v4, vcc
	v_sub_u32_e32 v4, v3, v2
	v_cndmask_b32_e32 v3, v3, v4, vcc
	v_add_u32_e32 v4, 1, v1
	v_cmp_ge_u32_e32 vcc, v3, v2
	v_add_u32_e32 v3, 1, v5
	s_nop 0
	v_cndmask_b32_e32 v1, v1, v4, vcc
	v_mul_lo_u32 v4, v2, v1
	v_add_u32_e32 v2, v4, v2
	v_cmp_ne_u32_e32 vcc, v3, v2
	s_and_saveexec_b64 s[4:5], vcc
	s_xor_b64 s[4:5], exec, s[4:5]
	s_cbranch_execz .LBB0_171
	s_waitcnt lgkmcnt(0)
	v_cmp_eq_u32_e32 vcc, v5, v4
	s_cbranch_vccz .Lxb_nf_0
	buffer_wbl2 sc1
.Lxb_nf_0:
	v_mov_b32_e32 v0, 0x3000
	global_load_dword v0, v0, s[56:57] offset:1280 sc1
	s_add_u32 s8, s56, 0x3500
	s_addc_u32 s9, s57, 0
	s_waitcnt vmcnt(0)
	v_cmp_eq_u32_e32 vcc, v0, v1
	s_and_saveexec_b64 s[6:7], vcc
	s_cbranch_execz .LBB0_170
	s_mov_b32 s3, 1
	s_mov_b64 s[10:11], 0
	v_mov_b32_e32 v0, 0
	s_branch .LBB0_161

.LBB0_782:
	s_or_b64 exec, exec, s[8:9]
	v_cvt_f32_u32_e32 v4, v2
	s_waitcnt vmcnt(0)
	v_readfirstlane_b32 s8, v3
	v_sub_u32_e32 v3, 0, v2
	v_rcp_iflag_f32_e32 v4, v4
	v_add_u32_e32 v5, s8, v1
	v_mul_f32_e32 v4, 0x4f7ffffe, v4
	v_cvt_u32_f32_e32 v4, v4
	v_mul_lo_u32 v1, v3, v4
	v_mul_hi_u32 v1, v4, v1
	v_add_u32_e32 v1, v4, v1
	v_mul_hi_u32 v1, v5, v1
	v_mul_lo_u32 v3, v1, v2
	v_sub_u32_e32 v3, v5, v3
	v_add_u32_e32 v4, 1, v1
	v_cmp_ge_u32_e32 vcc, v3, v2
	s_nop 1
	v_cndmask_b32_e32 v1, v1, v4, vcc
	v_sub_u32_e32 v4, v3, v2
	v_cndmask_b32_e32 v3, v3, v4, vcc
	v_add_u32_e32 v4, 1, v1
	v_cmp_ge_u32_e32 vcc, v3, v2
	v_add_u32_e32 v3, 1, v5
	s_nop 0
	v_cndmask_b32_e32 v1, v1, v4, vcc
	v_mul_lo_u32 v4, v2, v1
	v_add_u32_e32 v2, v4, v2
	v_cmp_ne_u32_e32 vcc, v3, v2
	s_and_saveexec_b64 s[8:9], vcc
	s_xor_b64 s[8:9], exec, s[8:9]
	s_cbranch_execz .LBB0_796
	s_waitcnt lgkmcnt(0)
	v_cmp_eq_u32_e32 vcc, v5, v4
	s_cbranch_vccz .Lxb_nf_5
	buffer_wbl2 sc1
.Lxb_nf_5:
	v_mov_b32_e32 v0, 0x3000
	global_load_dword v0, v0, s[56:57] offset:1280 sc1
	s_add_u32 s12, s56, 0x3500
	s_addc_u32 s13, s57, 0
	s_waitcnt vmcnt(0)
	v_cmp_eq_u32_e32 vcc, v0, v1
	s_and_saveexec_b64 s[10:11], vcc
	s_cbranch_execz .LBB0_795
	s_mov_b32 s33, 1
	s_mov_b64 s[14:15], 0
	v_mov_b32_e32 v0, 0
	s_branch .LBB0_786

.LBB0_1398:
	s_or_b64 exec, exec, s[10:11]
	v_cvt_f32_u32_e32 v4, v2
	s_waitcnt vmcnt(0)
	v_readfirstlane_b32 s10, v3
	v_sub_u32_e32 v3, 0, v2
	v_rcp_iflag_f32_e32 v4, v4
	v_add_u32_e32 v5, s10, v1
	v_mul_f32_e32 v4, 0x4f7ffffe, v4
	v_cvt_u32_f32_e32 v4, v4
	v_mul_lo_u32 v1, v3, v4
	v_mul_hi_u32 v1, v4, v1
	v_add_u32_e32 v1, v4, v1
	v_mul_hi_u32 v1, v5, v1
	v_mul_lo_u32 v3, v1, v2
	v_sub_u32_e32 v3, v5, v3
	v_add_u32_e32 v4, 1, v1
	v_cmp_ge_u32_e32 vcc, v3, v2
	s_nop 1
	v_cndmask_b32_e32 v1, v1, v4, vcc
	v_sub_u32_e32 v4, v3, v2
	v_cndmask_b32_e32 v3, v3, v4, vcc
	v_add_u32_e32 v4, 1, v1
	v_cmp_ge_u32_e32 vcc, v3, v2
	v_add_u32_e32 v3, 1, v5
	s_nop 0
	v_cndmask_b32_e32 v1, v1, v4, vcc
	v_mul_lo_u32 v4, v2, v1
	v_add_u32_e32 v2, v4, v2
	v_cmp_ne_u32_e32 vcc, v3, v2
	s_and_saveexec_b64 s[10:11], vcc
	s_xor_b64 s[10:11], exec, s[10:11]
	s_cbranch_execz .LBB0_1412
	s_waitcnt lgkmcnt(0)
	v_cmp_eq_u32_e32 vcc, v5, v4
	s_cbranch_vccz .Lxb_nf_10
	buffer_wbl2 sc1
.Lxb_nf_10:
	v_mov_b32_e32 v0, 0x3000
	global_load_dword v0, v0, s[56:57] offset:1280 sc1
	s_add_u32 s24, s56, 0x3500
	s_addc_u32 s25, s57, 0
	s_waitcnt vmcnt(0)
	v_cmp_eq_u32_e32 vcc, v0, v1
	s_and_saveexec_b64 s[12:13], vcc
	s_cbranch_execz .LBB0_1411
	s_mov_b32 s33, 1
	s_mov_b64 s[26:27], 0
	v_mov_b32_e32 v0, 0
	s_branch .LBB0_1402

.LBB0_1514:
	s_cmp_lt_i32 s58, 11
	s_cselect_b64 s[0:1], -1, 0
	s_cmp_gt_i32 s59, 10
	s_cselect_b64 s[4:5], -1, 0
	s_and_b64 s[0:1], s[0:1], s[4:5]
	s_andn2_b64 vcc, exec, s[0:1]
	s_cbranch_vccnz .LBB0_1518
	s_waitcnt vmcnt(4)
	v_mbcnt_lo_u32_b32 v0, -1, 0
	s_lshl_b32 s0, s2, 3
	v_mbcnt_hi_u32_b32 v0, -1, v0
	s_add_i32 s0, s84, s0
	v_mov_b32_e32 v1, v0
	s_cmpk_gt_i32 s0, 0x3fff
	s_cbranch_scc1 .LBB0_1518
	v_lshlrev_b32_e32 v2, 3, v1
	v_and_b32_e32 v1, 64, v0
	v_add_u32_e32 v1, 64, v1
	s_waitcnt vmcnt(0)
	v_xor_b32_e32 v18, 32, v0
	v_cmp_lt_i32_e32 vcc, v18, v1
	v_ashrrev_i32_e32 v3, 31, v2
	v_add_u32_e32 v12, 0xa00, v2
	v_cndmask_b32_e32 v18, v0, v18, vcc
	v_lshlrev_b32_e32 v242, 2, v18
	v_xor_b32_e32 v18, 16, v0
	v_cmp_lt_i32_e32 vcc, v18, v1
	s_ashr_i32 s1, s0, 31
	v_add_u32_e32 v6, 0x400, v2
	v_cndmask_b32_e32 v18, v0, v18, vcc
	v_lshlrev_b32_e32 v243, 2, v18
	v_xor_b32_e32 v18, 8, v0
	v_cmp_lt_i32_e32 vcc, v18, v1
	v_add_u32_e32 v10, 0x800, v2
	v_ashrrev_i32_e32 v13, 31, v12
	v_cndmask_b32_e32 v18, v0, v18, vcc
	v_lshlrev_b32_e32 v244, 2, v18
	v_xor_b32_e32 v18, 4, v0
	v_cmp_lt_i32_e32 vcc, v18, v1
	s_lshl_b64 s[10:11], s[0:1], 13
	v_ashrrev_i32_e32 v7, 31, v6
	v_cndmask_b32_e32 v18, v0, v18, vcc
	v_lshlrev_b32_e32 v245, 2, v18
	v_xor_b32_e32 v18, 2, v0
	v_cmp_lt_i32_e32 vcc, v18, v1
	v_add_u32_e32 v8, 0x600, v2
	v_ashrrev_i32_e32 v11, 31, v10
	v_cndmask_b32_e32 v18, v0, v18, vcc
	v_lshlrev_b32_e32 v246, 2, v18
	v_xor_b32_e32 v18, 1, v0
	v_cmp_lt_i32_e32 vcc, v18, v1
	s_mov_b64 s[12:13], 0xd400000
	v_ashrrev_i32_e32 v9, 31, v8
	v_cndmask_b32_e32 v0, v0, v18, vcc
	v_lshlrev_b32_e32 v247, 2, v0
	v_lshlrev_b64 v[0:1], 2, v[2:3]
	v_lshl_add_u64 v[20:21], s[52:53], 0, v[0:1]
	v_lshl_add_u64 v[54:55], s[54:55], 0, v[0:1]
	v_lshl_add_u64 v[0:1], v[12:13], 1, s[10:11]
	v_lshlrev_b64 v[18:19], 2, v[6:7]
	v_lshl_add_u64 v[56:57], v[0:1], 0, s[12:13]
	v_lshl_add_u64 v[0:1], v[10:11], 1, s[10:11]
	s_waitcnt lgkmcnt(0)
	v_lshlrev_b64 v[64:65], 2, v[8:9]
	v_lshl_add_u64 v[58:59], v[0:1], 0, s[12:13]
	v_lshl_add_u64 v[0:1], s[54:55], 0, v[18:19]
	v_add_u32_e32 v14, 0xc00, v2
	v_lshlrev_b64 v[66:67], 2, v[10:11]
	v_lshl_add_u64 v[60:61], v[0:1], 0, 16
	v_lshl_add_u64 v[0:1], s[54:55], 0, v[64:65]
	v_add_u32_e32 v4, 0x200, v2
	v_ashrrev_i32_e32 v15, 31, v14
	v_add_u32_e32 v16, 0xe00, v2
	v_lshl_add_u64 v[24:25], s[52:53], 0, v[64:65]
	v_lshlrev_b64 v[68:69], 2, v[12:13]
	v_lshl_add_u64 v[64:65], v[0:1], 0, 16
	v_lshl_add_u64 v[0:1], s[54:55], 0, v[66:67]
	v_ashrrev_i32_e32 v5, 31, v4
	v_ashrrev_i32_e32 v17, 31, v16
	v_lshl_add_u64 v[26:27], s[52:53], 0, v[66:67]
	v_lshlrev_b64 v[70:71], 2, v[14:15]
	s_lshl_b64 s[4:5], s[0:1], 14
	v_lshl_add_u64 v[66:67], v[0:1], 0, 16
	v_lshl_add_u64 v[0:1], s[54:55], 0, v[68:69]
	s_lshl_b32 s2, s34, 3
	v_lshl_add_u64 v[28:29], s[52:53], 0, v[68:69]
	v_lshlrev_b64 v[72:73], 2, v[16:17]
	v_lshl_add_u64 v[36:37], s[4:5], 0, v[4:5]
	v_lshl_add_u64 v[4:5], v[16:17], 1, s[10:11]
	v_lshl_add_u64 v[68:69], v[0:1], 0, 16
	v_lshl_add_u64 v[0:1], s[54:55], 0, v[70:71]
	v_lshl_add_u64 v[30:31], s[52:53], 0, v[70:71]
	s_ashr_i32 s3, s2, 31
	v_lshl_add_u64 v[50:51], v[4:5], 0, s[12:13]
	v_lshl_add_u64 v[4:5], v[14:15], 1, s[10:11]
	v_lshl_add_u64 v[70:71], v[0:1], 0, 16
	v_lshl_add_u64 v[0:1], s[54:55], 0, v[72:73]
	v_lshl_add_u64 v[22:23], s[52:53], 0, v[18:19]
	v_lshl_add_u64 v[32:33], s[52:53], 0, v[72:73]
	v_lshl_add_u64 v[34:35], s[4:5], 0, v[2:3]
	s_lshl_b64 s[6:7], s[2:3], 14
	v_lshl_add_u64 v[38:39], s[4:5], 0, v[6:7]
	v_lshl_add_u64 v[40:41], s[4:5], 0, v[8:9]
	v_lshl_add_u64 v[42:43], s[4:5], 0, v[10:11]
	v_lshl_add_u64 v[44:45], s[4:5], 0, v[12:13]
	v_lshl_add_u64 v[46:47], s[4:5], 0, v[14:15]
	v_lshl_add_u64 v[48:49], s[4:5], 0, v[16:17]
	s_lshl_b64 s[8:9], s[2:3], 13
	v_lshl_add_u64 v[52:53], v[4:5], 0, s[12:13]
	v_lshl_add_u64 v[62:63], v[2:3], 1, s[10:11]
	v_lshl_add_u64 v[72:73], v[0:1], 0, 16
	s_mov_b32 s1, 0xd400000
	s_mov_b32 s3, 0x1b801000
	s_mov_b32 s11, 0x1b803000
	s_mov_b32 s10, 0x3e000000
	v_mov_b32_e32 v248, 0x3727c5ac
	s_mov_b32 s12, 0x800000
	v_mbcnt_lo_u32_b32 v0, -1, 0
	v_mbcnt_hi_u32_b32 v0, -1, v0
	v_cmp_lt_u32_e32 vcc, 31, v0
	v_mov_b32_e32 v0, 0xfffffc10
	s_nop 1
	v_cndmask_b32_e64 v1, 0, -1, vcc
	v_and_b32_e32 v0, v0, v1
	v_lshl_add_u64 v[54:55], v[54:55], 0, v[0:1]
	v_lshl_add_u64 v[60:61], v[60:61], 0, v[0:1]
	v_lshl_add_u64 v[64:65], v[64:65], 0, v[0:1]
	v_lshl_add_u64 v[66:67], v[66:67], 0, v[0:1]
	v_lshl_add_u64 v[68:69], v[68:69], 0, v[0:1]
	v_lshl_add_u64 v[70:71], v[70:71], 0, v[0:1]
	v_lshl_add_u64 v[72:73], v[72:73], 0, v[0:1]
.LBB0_1517:
	v_lshl_add_u64 v[0:1], s[56:57], 0, v[62:63]
	v_add_co_u32_e32 v0, vcc, s1, v0
	v_lshl_add_u64 v[2:3], s[56:57], 0, v[34:35]
	s_nop 0
	v_addc_co_u32_e32 v1, vcc, 0, v1, vcc
	v_add_co_u32_e32 v82, vcc, s3, v2
	v_lshl_add_u64 v[4:5], s[56:57], 0, v[36:37]
	s_nop 0
	v_addc_co_u32_e32 v83, vcc, 0, v3, vcc
	v_add_co_u32_e32 v2, vcc, s11, v2
	v_lshl_add_u64 v[6:7], s[56:57], 0, v[38:39]
	s_nop 0
	v_addc_co_u32_e32 v3, vcc, 0, v3, vcc
	v_add_co_u32_e32 v84, vcc, s3, v4
	v_lshl_add_u64 v[8:9], s[56:57], 0, v[40:41]
	s_nop 0
	v_addc_co_u32_e32 v85, vcc, 0, v5, vcc
	v_add_co_u32_e32 v4, vcc, s11, v4
	v_lshl_add_u64 v[12:13], s[56:57], 0, v[42:43]
	s_nop 0
	v_addc_co_u32_e32 v5, vcc, 0, v5, vcc
	v_add_co_u32_e32 v86, vcc, s3, v6
	v_lshl_add_u64 v[16:17], s[56:57], 0, v[44:45]
	s_nop 0
	v_addc_co_u32_e32 v87, vcc, 0, v7, vcc
	v_add_co_u32_e32 v6, vcc, s11, v6
	v_lshl_add_u64 v[18:19], s[56:57], 0, v[46:47]
	s_nop 0
	v_addc_co_u32_e32 v7, vcc, 0, v7, vcc
	v_add_co_u32_e32 v88, vcc, s3, v8
	v_lshl_add_u64 v[80:81], s[56:57], 0, v[48:49]
	s_nop 0
	v_addc_co_u32_e32 v89, vcc, 0, v9, vcc
	v_add_co_u32_e32 v8, vcc, s11, v8
	v_lshl_add_u64 v[10:11], s[56:57], 0, v[58:59]
	s_nop 0
	v_addc_co_u32_e32 v9, vcc, 0, v9, vcc
	v_add_co_u32_e32 v90, vcc, s3, v12
	v_lshl_add_u64 v[14:15], s[56:57], 0, v[56:57]
	s_nop 0
	v_addc_co_u32_e32 v91, vcc, 0, v13, vcc
	v_add_co_u32_e32 v12, vcc, s11, v12
	v_lshl_add_u64 v[76:77], s[56:57], 0, v[52:53]
	s_nop 0
	v_addc_co_u32_e32 v13, vcc, 0, v13, vcc
	v_add_co_u32_e32 v92, vcc, s3, v16
	v_lshl_add_u64 v[78:79], s[56:57], 0, v[50:51]
	s_nop 0
	v_addc_co_u32_e32 v93, vcc, 0, v17, vcc
	v_add_co_u32_e32 v94, vcc, s11, v16
	global_load_dwordx2 v[112:113], v[82:83], off offset:-4096 nt
	global_load_dwordx2 v[114:115], v[82:83], off nt
	global_load_dwordx2 v[116:117], v[2:3], off offset:-4096 nt
	global_load_dwordx2 v[118:119], v[2:3], off nt
	global_load_dwordx2 v[122:123], v[84:85], off offset:-4096 nt
	global_load_dwordx2 v[124:125], v[84:85], off nt
	global_load_dwordx2 v[128:129], v[4:5], off offset:-4096 nt
	global_load_dwordx2 v[132:133], v[4:5], off nt
	global_load_dwordx4 v[100:103], v[0:1], off nt
	global_load_dwordx4 v[160:163], v[0:1], off offset:1024 nt
	global_load_dwordx4 v[168:171], v[0:1], off offset:2048 nt
	global_load_dwordx2 v[196:197], v[86:87], off offset:-4096 nt
	global_load_dwordx2 v[182:183], v[86:87], off nt
	global_load_dwordx2 v[174:175], v[6:7], off offset:-4096 nt
	global_load_dwordx2 v[158:159], v[6:7], off nt
	global_load_dwordx4 v[198:201], v[0:1], off offset:3072 nt
	global_load_dwordx2 v[164:165], v[88:89], off offset:-4096 nt
	global_load_dwordx2 v[166:167], v[88:89], off nt
	global_load_dwordx2 v[154:155], v[8:9], off offset:-4096 nt
	global_load_dwordx2 v[150:151], v[8:9], off nt
	v_addc_co_u32_e32 v95, vcc, 0, v17, vcc
	v_add_co_u32_e32 v96, vcc, s3, v18
	v_lshl_add_u64 v[74:75], v[54:55], 0, s[4:5]
	s_nop 0
	v_addc_co_u32_e32 v97, vcc, 0, v19, vcc
	v_add_co_u32_e32 v104, vcc, s11, v18
	s_add_i32 s0, s0, s2
	s_nop 0
	v_addc_co_u32_e32 v105, vcc, 0, v19, vcc
	v_add_co_u32_e32 v108, vcc, s3, v80
	v_lshl_add_u64 v[34:35], v[34:35], 0, s[6:7]
	s_nop 0
	v_addc_co_u32_e32 v109, vcc, 0, v81, vcc
	v_add_co_u32_e32 v110, vcc, s11, v80
	v_lshl_add_u64 v[36:37], v[36:37], 0, s[6:7]
	s_nop 0
	v_addc_co_u32_e32 v111, vcc, 0, v81, vcc
	global_load_dwordx2 v[146:147], v[90:91], off offset:-4096 nt
	global_load_dwordx2 v[142:143], v[90:91], off nt
	global_load_dwordx2 v[98:99], v[12:13], off offset:-4096 nt
	s_nop 0
	global_load_dwordx2 v[90:91], v[12:13], off nt
	global_load_dwordx4 v[236:239], v[10:11], off nt
	global_load_dwordx4 v[16:19], v[14:15], off nt
	global_load_dwordx2 v[140:141], v[92:93], off offset:-4096 nt
	global_load_dwordx2 v[136:137], v[92:93], off nt
	global_load_dwordx2 v[86:87], v[94:95], off offset:-4096 nt
	global_load_dwordx2 v[84:85], v[94:95], off nt
	global_load_dwordx2 v[134:135], v[96:97], off offset:-4096 nt
	global_load_dwordx2 v[126:127], v[96:97], off nt
	global_load_dwordx2 v[82:83], v[104:105], off offset:-4096 nt
	global_load_dwordx2 v[80:81], v[104:105], off nt
	global_load_dwordx4 v[12:15], v[76:77], off nt
	global_load_dwordx4 v[8:11], v[78:79], off nt
	global_load_dwordx2 v[106:107], v[108:109], off offset:-4096 nt
	s_nop 0
	global_load_dwordx2 v[108:109], v[108:109], off nt
	s_nop 0
	global_load_dwordx2 v[78:79], v[110:111], off offset:-4096 nt
	global_load_dwordx2 v[76:77], v[110:111], off nt
	global_load_dwordx4 v[0:3], v[20:21], off offset:16
	global_load_dwordx4 v[4:7], v[20:21], off
	v_lshl_add_u64 v[38:39], v[38:39], 0, s[6:7]
	v_lshl_add_u64 v[40:41], v[40:41], 0, s[6:7]
	v_lshl_add_u64 v[42:43], v[42:43], 0, s[6:7]
	v_lshl_add_u64 v[44:45], v[44:45], 0, s[6:7]
	v_lshl_add_u64 v[46:47], v[46:47], 0, s[6:7]
	v_lshl_add_u64 v[48:49], v[48:49], 0, s[6:7]
	v_lshl_add_u64 v[50:51], v[50:51], 0, s[8:9]
	v_lshl_add_u64 v[52:53], v[52:53], 0, s[8:9]
	v_lshl_add_u64 v[54:55], v[54:55], 0, s[6:7]
	v_lshl_add_u64 v[56:57], v[56:57], 0, s[8:9]
	v_lshl_add_u64 v[58:59], v[58:59], 0, s[8:9]
	v_lshl_add_u64 v[62:63], v[62:63], 0, s[8:9]
	s_cmpk_lt_i32 s0, 0x4000
	s_waitcnt vmcnt(41)
	v_cvt_pk_f32_fp8_e32 v[220:221], v113
	v_cvt_pk_f32_fp8_sdwa v[202:203], v112 src0_sel:WORD_1
	s_waitcnt vmcnt(40)
	v_cvt_pk_f32_fp8_e32 v[230:231], v115
	v_cvt_pk_f32_fp8_e32 v[204:205], v112
	v_cvt_pk_f32_fp8_sdwa v[216:217], v113 src0_sel:WORD_1
	v_cvt_pk_f32_fp8_sdwa v[208:209], v114 src0_sel:WORD_1
	v_cvt_pk_f32_fp8_e32 v[210:211], v114
	v_cvt_pk_f32_fp8_sdwa v[222:223], v115 src0_sel:WORD_1
	v_pk_add_f32 v[220:221], v[220:221], 0 op_sel_hi:[1,0]
	v_pk_add_f32 v[202:203], v[202:203], 0 op_sel_hi:[1,0]
	v_pk_add_f32 v[220:221], v[220:221], v[230:231]
	v_pk_add_f32 v[216:217], v[216:217], 0 op_sel_hi:[1,0]
	v_pk_add_f32 v[204:205], v[204:205], 0 op_sel_hi:[1,0]
	s_waitcnt vmcnt(32)
	v_lshlrev_b32_e32 v104, 16, v160
	v_and_b32_e32 v105, 0xffff0000, v160
	s_waitcnt vmcnt(30)
	v_cvt_pk_f32_fp8_e32 v[230:231], v197
	v_lshlrev_b32_e32 v110, 16, v161
	v_and_b32_e32 v111, 0xffff0000, v161
	v_cvt_pk_f32_fp8_sdwa v[250:251], v196 src0_sel:WORD_1
	v_pk_add_f32 v[202:203], v[202:203], v[208:209]
	s_waitcnt vmcnt(29)
	v_cvt_pk_f32_fp8_e32 v[208:209], v183
	v_pk_add_f32 v[216:217], v[216:217], v[222:223]
	v_cvt_pk_f32_fp8_e32 v[222:223], v182
	v_pk_add_f32 v[204:205], v[204:205], v[210:211]
	v_cvt_pk_f32_fp8_sdwa v[210:211], v182 src0_sel:WORD_1
	v_cvt_pk_f32_fp8_sdwa v[182:183], v183 src0_sel:WORD_1
	v_cvt_pk_f32_fp8_e32 v[212:213], v122
	v_cvt_pk_f32_fp8_e32 v[226:227], v123
	v_cvt_pk_f32_fp8_sdwa v[224:225], v123 src0_sel:WORD_1
	v_cvt_pk_f32_fp8_e32 v[218:219], v124
	v_pk_add_f32 v[230:231], v[230:231], 0 op_sel_hi:[1,0]
	v_cvt_pk_f32_fp8_e32 v[234:235], v125
	s_waitcnt vmcnt(17)
	v_lshlrev_b32_e32 v152, 16, v238
	v_and_b32_e32 v153, 0xffff0000, v238
	v_lshlrev_b32_e32 v160, 16, v239
	v_and_b32_e32 v161, 0xffff0000, v239
	v_cvt_pk_f32_fp8_sdwa v[232:233], v125 src0_sel:WORD_1
	v_pk_add_f32 v[208:209], v[230:231], v[208:209]
	v_cvt_pk_f32_fp8_e32 v[230:231], v165
	v_cvt_pk_f32_fp8_sdwa v[206:207], v122 src0_sel:WORD_1
	v_pk_add_f32 v[250:251], v[250:251], 0 op_sel_hi:[1,0]
	v_cvt_pk_f32_fp8_sdwa v[214:215], v124 src0_sel:WORD_1
	v_pk_add_f32 v[212:213], v[212:213], 0 op_sel_hi:[1,0]
	s_waitcnt vmcnt(6)
	v_lshlrev_b32_e32 v238, 16, v8
	v_and_b32_e32 v239, 0xffff0000, v8
	v_lshlrev_b32_e32 v240, 16, v9
	v_and_b32_e32 v241, 0xffff0000, v9
	v_cvt_pk_f32_fp8_e32 v[8:9], v196
	v_cvt_pk_f32_fp8_sdwa v[196:197], v197 src0_sel:WORD_1
	v_pk_add_f32 v[210:211], v[250:251], v[210:211]
	v_cvt_pk_f32_fp8_sdwa v[250:251], v167 src0_sel:WORD_1
	v_pk_add_f32 v[8:9], v[8:9], 0 op_sel_hi:[1,0]
	v_pk_add_f32 v[196:197], v[196:197], 0 op_sel_hi:[1,0]
	v_pk_add_f32 v[8:9], v[8:9], v[222:223]
	v_pk_add_f32 v[182:183], v[196:197], v[182:183]
	v_cvt_pk_f32_fp8_sdwa v[196:197], v165 src0_sel:WORD_1
	v_cvt_pk_f32_fp8_e32 v[222:223], v167
	v_cvt_pk_f32_fp8_e32 v[188:189], v117
	v_cvt_pk_f32_fp8_e32 v[190:191], v128
	v_cvt_pk_f32_fp8_sdwa v[186:187], v128 src0_sel:WORD_1
	v_pk_add_f32 v[226:227], v[226:227], 0 op_sel_hi:[1,0]
	v_pk_add_f32 v[224:225], v[224:225], 0 op_sel_hi:[1,0]
	v_pk_add_f32 v[212:213], v[212:213], v[218:219]
	v_cvt_pk_f32_fp8_e32 v[218:219], v175
	v_cvt_pk_f32_fp8_e32 v[180:181], v116
	v_cvt_pk_f32_fp8_sdwa v[184:185], v117 src0_sel:WORD_1
	v_pk_add_f32 v[226:227], v[226:227], v[234:235]
	v_cvt_pk_f32_fp8_e32 v[234:235], v174
	v_pk_add_f32 v[224:225], v[224:225], v[232:233]
	v_cvt_pk_f32_fp8_sdwa v[232:233], v174 src0_sel:WORD_1
	v_cvt_pk_f32_fp8_sdwa v[174:175], v175 src0_sel:WORD_1
	v_pk_add_f32 v[230:231], v[230:231], 0 op_sel_hi:[1,0]
	v_pk_add_f32 v[206:207], v[206:207], 0 op_sel_hi:[1,0]
	v_pk_add_f32 v[222:223], v[230:231], v[222:223]
	v_cvt_pk_f32_fp8_e32 v[230:231], v164
	v_pk_add_f32 v[196:197], v[196:197], 0 op_sel_hi:[1,0]
	v_pk_add_f32 v[206:207], v[206:207], v[214:215]
	v_pk_add_f32 v[196:197], v[196:197], v[250:251]
	v_cvt_pk_f32_fp8_e32 v[250:251], v166
	v_cvt_pk_f32_fp8_sdwa v[164:165], v164 src0_sel:WORD_1
	v_pk_add_f32 v[188:189], v[220:221], v[188:189]
	v_cvt_pk_f32_fp8_e32 v[220:221], v154
	v_pk_add_f32 v[190:191], v[212:213], v[190:191]
	v_cvt_pk_f32_fp8_e32 v[212:213], v146
	v_pk_add_f32 v[186:187], v[206:207], v[186:187]
	v_cvt_pk_f32_fp8_sdwa v[206:207], v146 src0_sel:WORD_1
	v_pk_add_f32 v[208:209], v[208:209], v[218:219]
	v_cvt_pk_f32_fp8_e32 v[218:219], v147
	v_cvt_pk_f32_fp8_sdwa v[146:147], v147 src0_sel:WORD_1
	v_cvt_pk_f32_fp8_sdwa v[166:167], v166 src0_sel:WORD_1
	v_pk_add_f32 v[184:185], v[216:217], v[184:185]
	v_cvt_pk_f32_fp8_sdwa v[216:217], v154 src0_sel:WORD_1
	v_pk_add_f32 v[180:181], v[204:205], v[180:181]
	v_cvt_pk_f32_fp8_e32 v[204:205], v155
	v_cvt_pk_f32_fp8_sdwa v[154:155], v155 src0_sel:WORD_1
	v_pk_add_f32 v[174:175], v[182:183], v[174:175]
	v_cvt_pk_f32_fp8_e32 v[182:183], v142
	v_pk_add_f32 v[8:9], v[8:9], v[234:235]
	v_cvt_pk_f32_fp8_sdwa v[234:235], v142 src0_sel:WORD_1
	v_pk_add_f32 v[210:211], v[210:211], v[232:233]
	v_cvt_pk_f32_fp8_e32 v[232:233], v143
	v_cvt_pk_f32_fp8_sdwa v[142:143], v143 src0_sel:WORD_1
	v_pk_add_f32 v[230:231], v[230:231], 0 op_sel_hi:[1,0]
	v_cvt_pk_f32_fp8_sdwa v[192:193], v129 src0_sel:WORD_1
	v_pk_add_f32 v[230:231], v[230:231], v[250:251]
	v_cvt_pk_f32_fp8_sdwa v[176:177], v116 src0_sel:WORD_1
	v_cvt_pk_f32_fp8_e32 v[194:195], v129
	v_pk_add_f32 v[164:165], v[164:165], 0 op_sel_hi:[1,0]
	v_pk_add_f32 v[220:221], v[230:231], v[220:221]
	v_cvt_pk_f32_fp8_e32 v[230:231], v141
	v_pk_add_f32 v[146:147], v[146:147], 0 op_sel_hi:[1,0]
	v_pk_add_f32 v[164:165], v[164:165], v[166:167]
	v_pk_add_f32 v[204:205], v[222:223], v[204:205]
	v_cvt_pk_f32_fp8_e32 v[222:223], v140
	v_pk_add_f32 v[154:155], v[196:197], v[154:155]
	v_cvt_pk_f32_fp8_sdwa v[196:197], v140 src0_sel:WORD_1
	v_cvt_pk_f32_fp8_sdwa v[140:141], v141 src0_sel:WORD_1
	v_pk_add_f32 v[218:219], v[218:219], 0 op_sel_hi:[1,0]
	v_pk_add_f32 v[142:143], v[146:147], v[142:143]
	v_cvt_pk_f32_fp8_e32 v[146:147], v137
	v_pk_add_f32 v[164:165], v[164:165], v[216:217]
	v_cvt_pk_f32_fp8_e32 v[216:217], v136
	v_pk_add_f32 v[218:219], v[218:219], v[232:233]
	v_cvt_pk_f32_fp8_sdwa v[232:233], v136 src0_sel:WORD_1
	v_cvt_pk_f32_fp8_sdwa v[136:137], v137 src0_sel:WORD_1
	v_cvt_pk_f32_fp8_e32 v[214:215], v158
	v_cvt_pk_f32_fp8_sdwa v[250:251], v158 src0_sel:WORD_1
	v_pk_add_f32 v[192:193], v[224:225], v[192:193]
	v_cvt_pk_f32_fp8_e32 v[224:225], v151
	v_pk_add_f32 v[176:177], v[202:203], v[176:177]
	v_cvt_pk_f32_fp8_e32 v[202:203], v150
	v_pk_add_f32 v[194:195], v[226:227], v[194:195]
	v_cvt_pk_f32_fp8_sdwa v[226:227], v150 src0_sel:WORD_1
	v_cvt_pk_f32_fp8_sdwa v[150:151], v151 src0_sel:WORD_1
	v_pk_add_f32 v[212:213], v[212:213], 0 op_sel_hi:[1,0]
	v_pk_add_f32 v[206:207], v[206:207], 0 op_sel_hi:[1,0]
	v_pk_add_f32 v[230:231], v[230:231], 0 op_sel_hi:[1,0]
	v_cvt_pk_f32_fp8_e32 v[114:115], v118
	v_cvt_pk_f32_fp8_e32 v[122:123], v132
	v_pk_add_f32 v[182:183], v[212:213], v[182:183]
	v_cvt_pk_f32_fp8_e32 v[212:213], v134
	v_pk_add_f32 v[206:207], v[206:207], v[234:235]
	v_cvt_pk_f32_fp8_sdwa v[234:235], v134 src0_sel:WORD_1
	v_pk_add_f32 v[146:147], v[230:231], v[146:147]
	v_cvt_pk_f32_fp8_e32 v[230:231], v135
	v_cvt_pk_f32_fp8_sdwa v[134:135], v135 src0_sel:WORD_1
	v_pk_add_f32 v[140:141], v[140:141], 0 op_sel_hi:[1,0]
	v_pk_add_f32 v[222:223], v[222:223], 0 op_sel_hi:[1,0]
	v_pk_add_f32 v[196:197], v[196:197], 0 op_sel_hi:[1,0]
	v_cvt_pk_f32_fp8_sdwa v[112:113], v118 src0_sel:WORD_1
	v_cvt_pk_f32_fp8_e32 v[166:167], v159
	v_cvt_pk_f32_fp8_sdwa v[158:159], v159 src0_sel:WORD_1
	v_pk_add_f32 v[136:137], v[140:141], v[136:137]
	v_cvt_pk_f32_fp8_e32 v[140:141], v126
	v_pk_add_f32 v[216:217], v[222:223], v[216:217]
	v_cvt_pk_f32_fp8_e32 v[222:223], v127
	v_pk_add_f32 v[196:197], v[196:197], v[232:233]
	v_cvt_pk_f32_fp8_sdwa v[232:233], v126 src0_sel:WORD_1
	v_cvt_pk_f32_fp8_sdwa v[126:127], v127 src0_sel:WORD_1
	v_pk_add_f32 v[8:9], v[8:9], v[214:215]
	v_cvt_pk_f32_fp8_e32 v[214:215], v82
	v_pk_add_f32 v[210:211], v[210:211], v[250:251]
	v_cvt_pk_f32_fp8_sdwa v[250:251], v82 src0_sel:WORD_1
	v_pk_add_f32 v[204:205], v[204:205], v[224:225]
	v_cvt_pk_f32_fp8_e32 v[224:225], v83
	v_cvt_pk_f32_fp8_sdwa v[82:83], v83 src0_sel:WORD_1
	v_cvt_pk_f32_fp8_e32 v[120:121], v119
	v_pk_add_f32 v[150:151], v[154:155], v[150:151]
	v_cvt_pk_f32_fp8_e32 v[154:155], v80
	v_cvt_pk_f32_fp8_e32 v[130:131], v133
	v_lshlrev_b32_e32 v94, 16, v100
	v_and_b32_e32 v95, 0xffff0000, v100
	v_pk_add_f32 v[134:135], v[134:135], 0 op_sel_hi:[1,0]
	v_pk_add_f32 v[212:213], v[212:213], 0 op_sel_hi:[1,0]
	v_pk_add_f32 v[114:115], v[180:181], v[114:115]
	v_pk_add_f32 v[122:123], v[190:191], v[122:123]
	v_cvt_pk_f32_fp8_e32 v[190:191], v87
	v_cvt_pk_f32_fp8_sdwa v[116:117], v119 src0_sel:WORD_1
	v_lshlrev_b32_e32 v96, 16, v101
	v_and_b32_e32 v97, 0xffff0000, v101
	v_lshlrev_b32_e32 v156, 16, v201
	v_and_b32_e32 v157, 0xffff0000, v201
	v_pk_add_f32 v[126:127], v[134:135], v[126:127]
	v_pk_add_f32 v[140:141], v[212:213], v[140:141]
	v_pk_add_f32 v[112:113], v[176:177], v[112:113]
	v_pk_add_f32 v[158:159], v[174:175], v[158:159]
	v_cvt_pk_f32_fp8_e32 v[174:175], v85
	v_pk_fma_f32 v[94:95], v[114:115], s[10:11], v[94:95] op_sel_hi:[1,0,1]
	v_pk_add_f32 v[82:83], v[126:127], v[82:83]
	v_pk_add_f32 v[126:127], v[140:141], v[214:215]
	v_pk_fma_f32 v[96:97], v[112:113], s[10:11], v[96:97] op_sel_hi:[1,0,1]
	v_pk_fma_f32 v[104:105], v[122:123], s[10:11], v[104:105] op_sel_hi:[1,0,1]
	v_pk_fma_f32 v[122:123], v[150:151], s[10:11], v[156:157] op_sel_hi:[1,0,1]
	v_pk_mul_f32 v[150:151], v[94:95], v[94:95]
	v_lshlrev_b32_e32 v88, 16, v102
	v_and_b32_e32 v89, 0xffff0000, v102
	v_pk_add_f32 v[120:121], v[188:189], v[120:121]
	v_pk_add_f32 v[126:127], v[126:127], v[154:155]
	v_pk_mul_f32 v[154:155], v[96:97], v[96:97]
	v_add_f32_e32 v150, v150, v151
	v_lshlrev_b32_e32 v100, 16, v162
	v_and_b32_e32 v101, 0xffff0000, v162
	v_pk_add_f32 v[130:131], v[194:195], v[130:131]
	v_pk_add_f32 v[146:147], v[146:147], v[190:191]
	v_pk_fma_f32 v[88:89], v[120:121], s[10:11], v[88:89] op_sel_hi:[1,0,1]
	v_add_f32_e32 v150, v150, v154
	v_cvt_pk_f32_fp8_sdwa v[118:119], v132 src0_sel:WORD_1
	v_lshlrev_b32_e32 v92, 16, v103
	v_and_b32_e32 v93, 0xffff0000, v103
	v_pk_add_f32 v[116:117], v[184:185], v[116:117]
	v_pk_fma_f32 v[100:101], v[130:131], s[10:11], v[100:101] op_sel_hi:[1,0,1]
	v_pk_add_f32 v[130:131], v[146:147], v[174:175]
	v_pk_mul_f32 v[146:147], v[88:89], v[88:89]
	v_add_f32_e32 v150, v155, v150
	v_cvt_pk_f32_fp8_sdwa v[128:129], v133 src0_sel:WORD_1
	v_lshlrev_b32_e32 v148, 16, v200
	v_and_b32_e32 v149, 0xffff0000, v200
	v_pk_fma_f32 v[92:93], v[116:117], s[10:11], v[92:93] op_sel_hi:[1,0,1]
	v_add_f32_e32 v146, v146, v150
	v_pk_fma_f32 v[120:121], v[204:205], s[10:11], v[148:149] op_sel_hi:[1,0,1]
	v_pk_mul_f32 v[148:149], v[92:93], v[92:93]
	v_add_f32_e32 v146, v147, v146
	v_lshlrev_b32_e32 v102, 16, v163
	v_and_b32_e32 v103, 0xffff0000, v163
	v_lshlrev_b32_e32 v124, 16, v170
	v_and_b32_e32 v125, 0xffff0000, v170
	v_lshlrev_b32_e32 v162, 16, v198
	v_and_b32_e32 v163, 0xffff0000, v198
	v_pk_add_f32 v[166:167], v[208:209], v[166:167]
	v_pk_add_f32 v[202:203], v[220:221], v[202:203]
	v_add_f32_e32 v146, v148, v146
	v_pk_add_f32 v[230:231], v[230:231], 0 op_sel_hi:[1,0]
	v_pk_add_f32 v[118:119], v[186:187], v[118:119]
	v_pk_fma_f32 v[112:113], v[166:167], s[10:11], v[124:125] op_sel_hi:[1,0,1]
	v_pk_fma_f32 v[124:125], v[202:203], s[10:11], v[162:163] op_sel_hi:[1,0,1]
	v_pk_mul_f32 v[162:163], v[104:105], v[104:105]
	v_add_f32_e32 v146, v149, v146
	v_lshlrev_b32_e32 v132, 16, v171
	v_and_b32_e32 v133, 0xffff0000, v171
	v_lshlrev_b32_e32 v170, 16, v199
	v_and_b32_e32 v171, 0xffff0000, v199
	v_pk_add_f32 v[222:223], v[230:231], v[222:223]
	s_waitcnt vmcnt(5)
	v_cvt_pk_f32_fp8_e32 v[230:231], v107
	v_pk_add_f32 v[128:129], v[192:193], v[128:129]
	v_pk_add_f32 v[164:165], v[164:165], v[226:227]
	v_pk_fma_f32 v[110:111], v[118:119], s[10:11], v[110:111] op_sel_hi:[1,0,1]
	v_add_f32_e32 v146, v146, v162
	v_cvt_pk_f32_fp8_sdwa v[134:135], v107 src0_sel:WORD_1
	s_waitcnt vmcnt(4)
	v_cvt_pk_f32_fp8_e32 v[212:213], v109
	v_pk_add_f32 v[234:235], v[234:235], 0 op_sel_hi:[1,0]
	v_pk_fma_f32 v[102:103], v[128:129], s[10:11], v[102:103] op_sel_hi:[1,0,1]
	v_pk_fma_f32 v[128:129], v[164:165], s[10:11], v[170:171] op_sel_hi:[1,0,1]
	v_pk_mul_f32 v[164:165], v[110:111], v[110:111]
	v_add_f32_e32 v146, v163, v146
	v_pk_add_f32 v[232:233], v[234:235], v[232:233]
	v_cvt_pk_f32_fp8_sdwa v[234:235], v109 src0_sel:WORD_1
	v_add_f32_e32 v146, v164, v146
	v_pk_mul_f32 v[156:157], v[100:101], v[100:101]
	v_add_f32_e32 v146, v165, v146
	v_pk_add_f32 v[230:231], v[230:231], 0 op_sel_hi:[1,0]
	v_cvt_pk_f32_fp8_e32 v[188:189], v99
	v_add_f32_e32 v146, v156, v146
	v_lshlrev_b32_e32 v138, 16, v168
	v_and_b32_e32 v139, 0xffff0000, v168
	v_pk_add_f32 v[212:213], v[230:231], v[212:213]
	v_cvt_pk_f32_fp8_e32 v[230:231], v106
	v_pk_add_f32 v[134:135], v[134:135], 0 op_sel_hi:[1,0]
	v_cvt_pk_f32_fp8_sdwa v[106:107], v106 src0_sel:WORD_1
	v_cvt_pk_f32_fp8_e32 v[176:177], v91
	v_pk_fma_f32 v[114:115], v[158:159], s[10:11], v[132:133] op_sel_hi:[1,0,1]
	v_pk_mul_f32 v[158:159], v[102:103], v[102:103]
	v_add_f32_e32 v146, v157, v146
	v_pk_add_f32 v[134:135], v[134:135], v[234:235]
	v_cvt_pk_f32_fp8_e32 v[234:235], v108
	v_cvt_pk_f32_fp8_sdwa v[108:109], v108 src0_sel:WORD_1
	v_pk_fma_f32 v[116:117], v[8:9], s[10:11], v[138:139] op_sel_hi:[1,0,1]
	v_add_f32_e32 v146, v158, v146
	v_lshlrev_b32_e32 v144, 16, v169
	v_and_b32_e32 v145, 0xffff0000, v169
	v_pk_mul_f32 v[174:175], v[116:117], v[116:117]
	v_add_f32_e32 v146, v159, v146
	v_pk_add_f32 v[188:189], v[218:219], v[188:189]
	v_pk_fma_f32 v[118:119], v[210:211], s[10:11], v[144:145] op_sel_hi:[1,0,1]
	v_add_f32_e32 v146, v146, v174
	v_pk_add_f32 v[230:231], v[230:231], 0 op_sel_hi:[1,0]
	v_pk_add_f32 v[106:107], v[106:107], 0 op_sel_hi:[1,0]
	v_pk_add_f32 v[8:9], v[188:189], v[176:177]
	v_pk_mul_f32 v[176:177], v[118:119], v[118:119]
	v_add_f32_e32 v146, v175, v146
	v_pk_add_f32 v[230:231], v[230:231], v[234:235]
	v_cvt_pk_f32_fp8_e32 v[234:235], v98
	v_pk_add_f32 v[106:107], v[106:107], v[108:109]
	v_cvt_pk_f32_fp8_sdwa v[108:109], v98 src0_sel:WORD_1
	v_cvt_pk_f32_fp8_sdwa v[98:99], v99 src0_sel:WORD_1
	v_add_f32_e32 v146, v176, v146
	v_cvt_pk_f32_fp8_e32 v[184:185], v90
	v_cvt_pk_f32_fp8_sdwa v[180:181], v90 src0_sel:WORD_1
	v_cvt_pk_f32_fp8_sdwa v[90:91], v91 src0_sel:WORD_1
	v_pk_mul_f32 v[166:167], v[112:113], v[112:113]
	v_add_f32_e32 v146, v177, v146
	v_cvt_pk_f32_fp8_e32 v[194:195], v86
	v_cvt_pk_f32_fp8_sdwa v[192:193], v86 src0_sel:WORD_1
	v_cvt_pk_f32_fp8_sdwa v[86:87], v87 src0_sel:WORD_1
	v_add_f32_e32 v146, v166, v146
	v_cvt_pk_f32_fp8_e32 v[186:187], v84
	v_cvt_pk_f32_fp8_sdwa v[208:209], v84 src0_sel:WORD_1
	v_cvt_pk_f32_fp8_sdwa v[84:85], v85 src0_sel:WORD_1
	v_pk_mul_f32 v[170:171], v[114:115], v[114:115]
	v_add_f32_e32 v146, v167, v146
	v_pk_add_f32 v[98:99], v[142:143], v[98:99]
	v_pk_add_f32 v[182:183], v[182:183], v[234:235]
	v_add_f32_e32 v146, v170, v146
	v_pk_add_f32 v[90:91], v[98:99], v[90:91]
	v_pk_add_f32 v[98:99], v[182:183], v[184:185]
	v_pk_mul_f32 v[184:185], v[124:125], v[124:125]
	v_add_f32_e32 v146, v171, v146
	v_pk_add_f32 v[86:87], v[136:137], v[86:87]
	v_pk_add_f32 v[194:195], v[216:217], v[194:195]
	v_add_f32_e32 v146, v146, v184
	v_pk_add_f32 v[84:85], v[86:87], v[84:85]
	v_pk_add_f32 v[86:87], v[194:195], v[186:187]
	v_pk_mul_f32 v[186:187], v[128:129], v[128:129]
	v_add_f32_e32 v146, v185, v146
	v_pk_add_f32 v[108:109], v[206:207], v[108:109]
	v_add_f32_e32 v146, v186, v146
	v_cvt_pk_f32_fp8_sdwa v[220:221], v80 src0_sel:WORD_1
	v_cvt_pk_f32_fp8_e32 v[226:227], v81
	v_cvt_pk_f32_fp8_sdwa v[80:81], v81 src0_sel:WORD_1
	s_waitcnt vmcnt(3)
	v_cvt_pk_f32_fp8_sdwa v[142:143], v78 src0_sel:WORD_1
	v_pk_add_f32 v[108:109], v[108:109], v[180:181]
	v_pk_mul_f32 v[180:181], v[120:121], v[120:121]
	v_add_f32_e32 v146, v187, v146
	v_add_f32_e32 v146, v180, v146
	v_lshlrev_b32_e32 v168, 16, v236
	v_and_b32_e32 v169, 0xffff0000, v236
	v_pk_mul_f32 v[182:183], v[122:123], v[122:123]
	v_add_f32_e32 v146, v181, v146
	v_lshlrev_b32_e32 v178, 16, v18
	v_and_b32_e32 v179, 0xffff0000, v18
	s_waitcnt vmcnt(2)
	v_cvt_pk_f32_fp8_sdwa v[190:191], v76 src0_sel:WORD_1
	v_pk_fma_f32 v[98:99], v[98:99], s[10:11], v[168:169] op_sel_hi:[1,0,1]
	v_add_f32_e32 v146, v182, v146
	v_lshlrev_b32_e32 v172, 16, v237
	v_and_b32_e32 v173, 0xffff0000, v237
	v_pk_add_f32 v[192:193], v[196:197], v[192:193]
	v_pk_add_f32 v[106:107], v[106:107], v[142:143]
	v_pk_add_f32 v[142:143], v[82:83], v[80:81]
	v_pk_fma_f32 v[80:81], v[130:131], s[10:11], v[178:179] op_sel_hi:[1,0,1]
	v_pk_mul_f32 v[130:131], v[98:99], v[98:99]
	v_add_f32_e32 v146, v183, v146
	v_lshlrev_b32_e32 v18, 16, v19
	v_and_b32_e32 v19, 0xffff0000, v19
	v_lshlrev_b32_e32 v198, 16, v16
	v_and_b32_e32 v199, 0xffff0000, v16
	v_lshlrev_b32_e32 v16, 16, v17
	v_and_b32_e32 v17, 0xffff0000, v17
	v_cvt_pk_f32_fp8_e32 v[218:219], v78
	v_cvt_pk_f32_fp8_e32 v[234:235], v79
	v_cvt_pk_f32_fp8_sdwa v[78:79], v79 src0_sel:WORD_1
	v_pk_add_f32 v[132:133], v[192:193], v[208:209]
	v_pk_fma_f32 v[108:109], v[108:109], s[10:11], v[172:173] op_sel_hi:[1,0,1]
	v_add_f32_e32 v130, v146, v130
	v_cvt_pk_f32_fp8_e32 v[206:207], v76
	v_cvt_pk_f32_fp8_e32 v[136:137], v77
	v_cvt_pk_f32_fp8_sdwa v[76:77], v77 src0_sel:WORD_1
	v_pk_fma_f32 v[82:83], v[84:85], s[10:11], v[18:19] op_sel_hi:[1,0,1]
	v_pk_fma_f32 v[84:85], v[86:87], s[10:11], v[198:199] op_sel_hi:[1,0,1]
	v_pk_fma_f32 v[86:87], v[132:133], s[10:11], v[16:17] op_sel_hi:[1,0,1]
	v_pk_mul_f32 v[132:133], v[108:109], v[108:109]
	v_add_f32_e32 v130, v131, v130
	v_lshlrev_b32_e32 v200, 16, v14
	v_and_b32_e32 v201, 0xffff0000, v14
	v_lshlrev_b32_e32 v14, 16, v15
	v_and_b32_e32 v15, 0xffff0000, v15
	v_pk_add_f32 v[106:107], v[106:107], v[190:191]
	v_pk_fma_f32 v[152:153], v[8:9], s[10:11], v[152:153] op_sel_hi:[1,0,1]
	v_add_f32_e32 v130, v132, v130
	v_pk_fma_f32 v[18:19], v[142:143], s[10:11], v[14:15] op_sel_hi:[1,0,1]
	v_pk_fma_f32 v[14:15], v[106:107], s[10:11], v[240:241] op_sel_hi:[1,0,1]
	v_pk_mul_f32 v[106:107], v[152:153], v[152:153]
	v_add_f32_e32 v130, v133, v130
	v_lshlrev_b32_e32 v228, 16, v12
	v_and_b32_e32 v229, 0xffff0000, v12
	v_pk_add_f32 v[78:79], v[134:135], v[78:79]
	v_pk_fma_f32 v[90:91], v[90:91], s[10:11], v[160:161] op_sel_hi:[1,0,1]
	v_add_f32_e32 v106, v106, v130
	v_pk_add_f32 v[196:197], v[222:223], v[224:225]
	v_pk_add_f32 v[144:145], v[78:79], v[76:77]
	v_pk_fma_f32 v[76:77], v[126:127], s[10:11], v[228:229] op_sel_hi:[1,0,1]
	v_pk_mul_f32 v[126:127], v[90:91], v[90:91]
	v_add_f32_e32 v106, v107, v106
	v_pk_add_f32 v[138:139], v[196:197], v[226:227]
	v_add_f32_e32 v106, v126, v106
	v_pk_add_f32 v[140:141], v[232:233], v[250:251]
	v_pk_fma_f32 v[16:17], v[138:139], s[10:11], v[200:201] op_sel_hi:[1,0,1]
	v_pk_mul_f32 v[138:139], v[84:85], v[84:85]
	v_add_f32_e32 v106, v127, v106
	v_lshlrev_b32_e32 v12, 16, v13
	v_and_b32_e32 v13, 0xffff0000, v13
	v_pk_add_f32 v[140:141], v[140:141], v[220:221]
	v_add_f32_e32 v106, v106, v138
	v_pk_add_f32 v[134:135], v[230:231], v[218:219]
	v_pk_fma_f32 v[78:79], v[140:141], s[10:11], v[12:13] op_sel_hi:[1,0,1]
	v_pk_mul_f32 v[140:141], v[86:87], v[86:87]
	v_add_f32_e32 v106, v139, v106
	v_pk_add_f32 v[134:135], v[134:135], v[206:207]
	v_add_f32_e32 v106, v140, v106
	v_pk_add_f32 v[212:213], v[212:213], v[234:235]
	v_pk_fma_f32 v[12:13], v[134:135], s[10:11], v[238:239] op_sel_hi:[1,0,1]
	v_pk_mul_f32 v[134:135], v[80:81], v[80:81]
	v_add_f32_e32 v106, v141, v106
	v_lshlrev_b32_e32 v236, 16, v10
	v_and_b32_e32 v237, 0xffff0000, v10
	v_pk_add_f32 v[136:137], v[212:213], v[136:137]
	v_add_f32_e32 v106, v134, v106
	v_pk_fma_f32 v[8:9], v[136:137], s[10:11], v[236:237] op_sel_hi:[1,0,1]
	v_pk_mul_f32 v[136:137], v[82:83], v[82:83]
	v_add_f32_e32 v106, v135, v106
	v_add_f32_e32 v106, v136, v106
	v_pk_mul_f32 v[160:161], v[76:77], v[76:77]
	v_add_f32_e32 v106, v137, v106
	v_add_f32_e32 v106, v106, v160
	v_pk_mul_f32 v[168:169], v[78:79], v[78:79]
	v_add_f32_e32 v106, v161, v106
	v_add_f32_e32 v106, v168, v106
	v_pk_mul_f32 v[142:143], v[16:17], v[16:17]
	v_add_f32_e32 v106, v169, v106
	v_lshlrev_b32_e32 v10, 16, v11
	v_and_b32_e32 v11, 0xffff0000, v11
	v_add_f32_e32 v106, v142, v106
	v_pk_fma_f32 v[10:11], v[144:145], s[10:11], v[10:11] op_sel_hi:[1,0,1]
	v_pk_mul_f32 v[144:145], v[18:19], v[18:19]
	v_add_f32_e32 v106, v143, v106
	v_add_f32_e32 v106, v144, v106
	v_pk_mul_f32 v[188:189], v[12:13], v[12:13]
	v_add_f32_e32 v106, v145, v106
	v_add_f32_e32 v106, v106, v188
	v_pk_mul_f32 v[190:191], v[14:15], v[14:15]
	v_add_f32_e32 v106, v189, v106
	v_add_f32_e32 v106, v190, v106
	v_pk_mul_f32 v[172:173], v[8:9], v[8:9]
	v_add_f32_e32 v106, v191, v106
	v_add_f32_e32 v106, v172, v106
	v_pk_mul_f32 v[178:179], v[10:11], v[10:11]
	v_add_f32_e32 v106, v173, v106
	v_add_f32_e32 v106, v178, v106
	v_add_f32_e32 v106, v179, v106
	global_load_dwordx4 v[160:163], v[20:21], off offset:2048
	global_load_dwordx4 v[164:167], v[20:21], off offset:2064
	global_load_dwordx4 v[168:171], v[22:23], off
	global_load_dwordx4 v[172:175], v[22:23], off offset:16
	global_load_dwordx4 v[176:179], v[24:25], off
	global_load_dwordx4 v[180:183], v[24:25], off offset:16
	global_load_dwordx4 v[184:187], v[26:27], off
	global_load_dwordx4 v[188:191], v[26:27], off offset:16
	global_load_dwordx4 v[192:195], v[28:29], off
	global_load_dwordx4 v[196:199], v[28:29], off offset:16
	global_load_dwordx4 v[200:203], v[30:31], off
	global_load_dwordx4 v[204:207], v[30:31], off offset:16
	global_load_dwordx4 v[208:211], v[32:33], off
	global_load_dwordx4 v[212:215], v[32:33], off offset:16
	ds_bpermute_b32 v107, v242, v106
	s_waitcnt lgkmcnt(0)
	v_add_f32_e32 v106, v106, v107
	ds_bpermute_b32 v107, v243, v106
	s_waitcnt lgkmcnt(0)
	v_add_f32_e32 v106, v106, v107
	ds_bpermute_b32 v107, v244, v106
	s_waitcnt lgkmcnt(0)
	v_add_f32_e32 v106, v106, v107
	ds_bpermute_b32 v107, v245, v106
	s_waitcnt lgkmcnt(0)
	v_add_f32_e32 v106, v106, v107
	ds_bpermute_b32 v107, v246, v106
	s_waitcnt lgkmcnt(0)
	v_add_f32_e32 v106, v106, v107
	ds_bpermute_b32 v107, v247, v106
	s_waitcnt lgkmcnt(0)
	v_add_f32_e32 v106, v106, v107
	v_fmamk_f32 v106, v106, 0x39800000, v248
	v_mul_f32_e32 v107, 0x4b800000, v106
	v_cmp_gt_f32_e32 vcc, s12, v106
	s_nop 1
	v_cndmask_b32_e32 v106, v106, v107, vcc
	v_rsq_f32_e32 v106, v106
	s_nop 0
	v_mul_f32_e32 v107, 0x45800000, v106
	v_cndmask_b32_e32 v106, v106, v107, vcc
	v_pk_mul_f32 v[94:95], v[94:95], v[106:107] op_sel_hi:[1,0]
	v_pk_mul_f32 v[96:97], v[96:97], v[106:107] op_sel_hi:[1,0]
	v_pk_mul_f32 v[88:89], v[88:89], v[106:107] op_sel_hi:[1,0]
	v_pk_mul_f32 v[92:93], v[92:93], v[106:107] op_sel_hi:[1,0]
	s_waitcnt vmcnt(14)
	v_pk_mul_f32 v[6:7], v[6:7], v[96:97]
	v_pk_mul_f32 v[4:5], v[4:5], v[94:95]
	v_pk_mul_f32 v[2:3], v[2:3], v[92:93]
	v_pk_mul_f32 v[0:1], v[0:1], v[88:89]
	s_nop 1
	v_permlane32_swap_b32_e32 v4, v0
	v_permlane32_swap_b32_e32 v5, v1
	v_permlane32_swap_b32_e32 v6, v2
	v_permlane32_swap_b32_e32 v7, v3
	global_store_dwordx4 v[74:75], v[4:7], off
	global_store_dwordx4 v[74:75], v[0:3], off offset:1024
	v_pk_mul_f32 v[88:89], v[110:111], v[106:107] op_sel_hi:[1,0]
	v_pk_mul_f32 v[92:93], v[104:105], v[106:107] op_sel_hi:[1,0]
	v_pk_mul_f32 v[94:95], v[102:103], v[106:107] op_sel_hi:[1,0]
	v_pk_mul_f32 v[96:97], v[100:101], v[106:107] op_sel_hi:[1,0]
	v_pk_mul_f32 v[90:91], v[90:91], v[106:107] op_sel_hi:[1,0]
	v_pk_mul_f32 v[86:87], v[86:87], v[106:107] op_sel_hi:[1,0]
	v_pk_mul_f32 v[84:85], v[84:85], v[106:107] op_sel_hi:[1,0]
	v_pk_mul_f32 v[82:83], v[82:83], v[106:107] op_sel_hi:[1,0]
	v_pk_mul_f32 v[80:81], v[80:81], v[106:107] op_sel_hi:[1,0]
	v_pk_mul_f32 v[78:79], v[78:79], v[106:107] op_sel_hi:[1,0]
	v_pk_mul_f32 v[76:77], v[76:77], v[106:107] op_sel_hi:[1,0]
	v_pk_mul_f32 v[18:19], v[18:19], v[106:107] op_sel_hi:[1,0]
	v_pk_mul_f32 v[16:17], v[16:17], v[106:107] op_sel_hi:[1,0]
	v_pk_mul_f32 v[14:15], v[14:15], v[106:107] op_sel_hi:[1,0]
	v_pk_mul_f32 v[12:13], v[12:13], v[106:107] op_sel_hi:[1,0]
	v_pk_mul_f32 v[10:11], v[10:11], v[106:107] op_sel_hi:[1,0]
	v_pk_mul_f32 v[8:9], v[8:9], v[106:107] op_sel_hi:[1,0]
	s_waitcnt vmcnt(14)
	v_pk_mul_f32 v[160:161], v[160:161], v[92:93]
	v_pk_mul_f32 v[162:163], v[162:163], v[88:89]
	s_waitcnt vmcnt(14)
	v_pk_mul_f32 v[164:165], v[164:165], v[96:97]
	v_pk_mul_f32 v[166:167], v[166:167], v[94:95]
	s_nop 1
	v_permlane32_swap_b32_e32 v160, v164
	v_permlane32_swap_b32_e32 v161, v165
	v_permlane32_swap_b32_e32 v162, v166
	v_permlane32_swap_b32_e32 v163, v167
	global_store_dwordx4 v[74:75], v[160:163], off offset:2048
	global_store_dwordx4 v[74:75], v[164:167], off offset:3072
	v_pk_mul_f32 v[88:89], v[118:119], v[106:107] op_sel_hi:[1,0]
	v_pk_mul_f32 v[92:93], v[116:117], v[106:107] op_sel_hi:[1,0]
	v_lshl_add_u64 v[74:75], v[60:61], 0, s[4:5]
	v_pk_mul_f32 v[94:95], v[114:115], v[106:107] op_sel_hi:[1,0]
	v_pk_mul_f32 v[96:97], v[112:113], v[106:107] op_sel_hi:[1,0]
	v_lshl_add_u64 v[60:61], v[60:61], 0, s[6:7]
	s_waitcnt vmcnt(14)
	v_pk_mul_f32 v[168:169], v[168:169], v[92:93]
	v_pk_mul_f32 v[170:171], v[170:171], v[88:89]
	s_waitcnt vmcnt(14)
	v_pk_mul_f32 v[172:173], v[172:173], v[96:97]
	v_pk_mul_f32 v[174:175], v[174:175], v[94:95]
	s_nop 1
	v_permlane32_swap_b32_e32 v168, v172
	v_permlane32_swap_b32_e32 v169, v173
	v_permlane32_swap_b32_e32 v170, v174
	v_permlane32_swap_b32_e32 v171, v175
	global_store_dwordx4 v[74:75], v[168:171], off offset:-16
	global_store_dwordx4 v[74:75], v[172:175], off offset:1008
	v_pk_mul_f32 v[88:89], v[128:129], v[106:107] op_sel_hi:[1,0]
	v_pk_mul_f32 v[92:93], v[124:125], v[106:107] op_sel_hi:[1,0]
	v_lshl_add_u64 v[74:75], v[64:65], 0, s[4:5]
	v_pk_mul_f32 v[94:95], v[122:123], v[106:107] op_sel_hi:[1,0]
	v_pk_mul_f32 v[96:97], v[120:121], v[106:107] op_sel_hi:[1,0]
	v_lshl_add_u64 v[64:65], v[64:65], 0, s[6:7]
	s_waitcnt vmcnt(14)
	v_pk_mul_f32 v[176:177], v[176:177], v[92:93]
	v_pk_mul_f32 v[178:179], v[178:179], v[88:89]
	s_waitcnt vmcnt(14)
	v_pk_mul_f32 v[180:181], v[180:181], v[96:97]
	v_pk_mul_f32 v[182:183], v[182:183], v[94:95]
	s_nop 1
	v_permlane32_swap_b32_e32 v176, v180
	v_permlane32_swap_b32_e32 v177, v181
	v_permlane32_swap_b32_e32 v178, v182
	v_permlane32_swap_b32_e32 v179, v183
	global_store_dwordx4 v[74:75], v[176:179], off offset:-16
	global_store_dwordx4 v[74:75], v[180:183], off offset:1008
	v_pk_mul_f32 v[88:89], v[108:109], v[106:107] op_sel_hi:[1,0]
	v_pk_mul_f32 v[92:93], v[98:99], v[106:107] op_sel_hi:[1,0]
	v_lshl_add_u64 v[74:75], v[66:67], 0, s[4:5]
	v_pk_mul_f32 v[94:95], v[152:153], v[106:107] op_sel_hi:[1,0]
	v_lshl_add_u64 v[66:67], v[66:67], 0, s[6:7]
	s_waitcnt vmcnt(14)
	v_pk_mul_f32 v[184:185], v[92:93], v[184:185]
	v_pk_mul_f32 v[186:187], v[88:89], v[186:187]
	s_waitcnt vmcnt(14)
	v_pk_mul_f32 v[188:189], v[94:95], v[188:189]
	v_pk_mul_f32 v[190:191], v[90:91], v[190:191]
	s_nop 1
	v_permlane32_swap_b32_e32 v184, v188
	v_permlane32_swap_b32_e32 v185, v189
	v_permlane32_swap_b32_e32 v186, v190
	v_permlane32_swap_b32_e32 v187, v191
	global_store_dwordx4 v[74:75], v[184:187], off offset:-16
	global_store_dwordx4 v[74:75], v[188:191], off offset:1008
	s_nop 1
	v_lshl_add_u64 v[74:75], v[68:69], 0, s[4:5]
	v_lshl_add_u64 v[68:69], v[68:69], 0, s[6:7]
	s_waitcnt vmcnt(14)
	v_pk_mul_f32 v[192:193], v[84:85], v[192:193]
	v_pk_mul_f32 v[194:195], v[86:87], v[194:195]
	s_waitcnt vmcnt(14)
	v_pk_mul_f32 v[196:197], v[80:81], v[196:197]
	v_pk_mul_f32 v[198:199], v[82:83], v[198:199]
	s_nop 1
	v_permlane32_swap_b32_e32 v192, v196
	v_permlane32_swap_b32_e32 v193, v197
	v_permlane32_swap_b32_e32 v194, v198
	v_permlane32_swap_b32_e32 v195, v199
	global_store_dwordx4 v[74:75], v[192:195], off offset:-16
	global_store_dwordx4 v[74:75], v[196:199], off offset:1008
	s_nop 1
	v_lshl_add_u64 v[74:75], v[70:71], 0, s[4:5]
	v_lshl_add_u64 v[70:71], v[70:71], 0, s[6:7]
	s_waitcnt vmcnt(14)
	v_pk_mul_f32 v[200:201], v[76:77], v[200:201]
	v_pk_mul_f32 v[202:203], v[78:79], v[202:203]
	s_waitcnt vmcnt(14)
	v_pk_mul_f32 v[204:205], v[16:17], v[204:205]
	v_pk_mul_f32 v[206:207], v[18:19], v[206:207]
	s_nop 1
	v_permlane32_swap_b32_e32 v200, v204
	v_permlane32_swap_b32_e32 v201, v205
	v_permlane32_swap_b32_e32 v202, v206
	v_permlane32_swap_b32_e32 v203, v207
	global_store_dwordx4 v[74:75], v[200:203], off offset:-16
	global_store_dwordx4 v[74:75], v[204:207], off offset:1008
	s_nop 1
	v_lshl_add_u64 v[16:17], v[72:73], 0, s[4:5]
	v_lshl_add_u64 v[72:73], v[72:73], 0, s[6:7]
	s_waitcnt vmcnt(14)
	v_pk_mul_f32 v[208:209], v[12:13], v[208:209]
	v_pk_mul_f32 v[210:211], v[14:15], v[210:211]
	s_waitcnt vmcnt(14)
	v_pk_mul_f32 v[212:213], v[8:9], v[212:213]
	v_pk_mul_f32 v[214:215], v[10:11], v[214:215]
	s_nop 1
	v_permlane32_swap_b32_e32 v208, v212
	v_permlane32_swap_b32_e32 v209, v213
	v_permlane32_swap_b32_e32 v210, v214
	v_permlane32_swap_b32_e32 v211, v215
	global_store_dwordx4 v[16:17], v[208:211], off offset:-16
	global_store_dwordx4 v[16:17], v[212:215], off offset:1008
	s_cbranch_scc1 .LBB0_1517
